# prep transposes: weight pointer read with one indexed scalar load (kernarg offset 8+8z) instead of a 4-branch ladder with two dependent scalar loads
# baseline (speedup 1.0000x reference)
.LBB13_5:
	s_andn2_b64 vcc, exec, s[4:5]
	s_cbranch_vccnz .LBB13_17
	s_load_dwordx4 s[4:7], s[0:1], 0x68
	s_add_i32 s14, s2, 0xffffff00
	s_lshr_b32 s15, s14, 8
	s_lshl_b32 s10, s15, 3
	s_add_u32 s10, s10, 8
	s_load_dwordx2 s[8:9], s[0:1], s10
